# speedup vs baseline: 1.0034x; 1.0034x over previous
.Lno_anc:
	s_or_b64 exec, exec, s[8:9]
	v_mov_b32_e32 v7, 0x80
	s_waitcnt vmcnt(0)
	s_sub_u32 s26, 0xff, s2
	s_mul_i32 s26, s26, 28
	s_lshr_b32 s26, s26, 7
	s_min_u32 s26, s26, 64
	s_cmp_eq_u32 s26, 0
	s_cbranch_scc1 .Lhold_done
